# s17 with the pre-pass helper items (cumsum, block means) back on raw blockIdx (even spread over XCDs); x1/x3/x2 keep the XCD-contiguous index
# baseline (speedup 1.0000x reference)
; #define PG8_LAS __attribute__((address_space(3)))
; #define LAS __attribute__((address_space(3)))
; __global__ void __launch_bounds__(NTHREADS, 2) mega(MArgs a) {
;     extern __shared__ __attribute__((aligned(16))) unsigned char lds[];
;     PG8_LAS unsigned char* L = (PG8_LAS unsigned char*)lds;
;     unsigned char* ws = a.ws;
;     for (int u = threadIdx.x; u < (MK_LDS_BYTES - LDSCTL_OFF) / 4; u += NTHREADS) ((LAS unsigned*)(L + LDSCTL_OFF))[u] = 0u;
;     __syncthreads();
;     XcdBarrier bar = xcd_barrier_post((unsigned*)(ws + WS_CTL) + CW_BAR, (volatile LAS unsigned*)(L + MISC_OFF) + 8);
.LBB0_12:
	s_load_dwordx2 s[14:15], s[0:1], 0x68
	s_load_dwordx2 s[12:13], s[0:1], 0x60
	s_load_dwordx16 s[36:51], s[0:1], 0x0
	v_lshrrev_b32_e32 v1, 20, v0
	v_lshrrev_b32_e32 v0, 10, v0
	s_waitcnt lgkmcnt(0)
	s_add_i32 s2, s14, 1
	s_cmpk_gt_i32 s15, 0x3e8
	v_writelane_b32 v252, s2, 13
	s_cselect_b64 s[2:3], -1, 0
	s_add_u32 s6, s0, 0x70
	s_addc_u32 s7, s1, 0
	s_add_u32 s82, s12, 0x4200
	v_writelane_b32 v252, s6, 14
	s_addc_u32 s83, s13, 0
	v_or_b32_e32 v0, v0, v1
	v_writelane_b32 v252, s7, 15
	s_add_u32 s6, s12, 0x4400
	s_addc_u32 s7, s13, 0
	v_writelane_b32 v252, s6, 16
	v_and_b32_e32 v250, 63, v243
	v_mov_b32_e32 v97, 0
	v_writelane_b32 v252, s7, 17
	s_add_u32 s6, s12, 0x4500
	s_addc_u32 s7, s13, 0
	v_writelane_b32 v252, s6, 18
	v_mov_b32_e32 v242, 0x358637bd
	v_mov_b32_e32 v248, 0xff800000
	v_writelane_b32 v252, s7, 19
	s_add_u32 s6, s12, 0x4600
	s_addc_u32 s7, s13, 0
	v_writelane_b32 v252, s6, 20
	v_mov_b32_e32 v249, 0xe0000
	v_mov_b32_e32 v244, 0x41b17218
	v_writelane_b32 v252, s7, 21
	s_add_u32 s6, s12, 0x4700
	s_addc_u32 s7, s13, 0
	v_writelane_b32 v252, s6, 22
	s_movk_i32 s27, 0x2000
	s_movk_i32 s91, 0x3800
	v_writelane_b32 v252, s7, 23
	s_add_u32 s6, s12, 0x4800
	s_addc_u32 s7, s13, 0
	v_writelane_b32 v252, s6, 24
	s_mov_b32 s96, 0x38000
	s_mov_b32 s97, 0x3fffffc
	v_writelane_b32 v252, s7, 25
	s_add_u32 s6, s12, 0x4900
	s_addc_u32 s7, s13, 0
	v_writelane_b32 v252, s6, 26
	s_mov_b32 s29, 0
	s_mov_b64 s[30:31], 0xe0000
	v_writelane_b32 v252, s7, 27
	s_add_u32 s6, s12, 0x4a00
	s_addc_u32 s7, s13, 0
	v_writelane_b32 v252, s6, 28
	s_mov_b64 s[62:63], 0x80
	s_nop 0
	v_writelane_b32 v252, s7, 29
	s_add_u32 s6, s12, 0x4b00
	s_addc_u32 s7, s13, 0
	v_writelane_b32 v252, s6, 30
	s_nop 1
	v_writelane_b32 v252, s7, 31
	s_add_u32 s6, s12, 0x4c00
	s_addc_u32 s7, s13, 0
	v_writelane_b32 v252, s6, 32
	s_nop 1
	v_writelane_b32 v252, s7, 33
	s_add_u32 s6, s12, 0x4d00
	s_addc_u32 s7, s13, 0
	v_writelane_b32 v252, s6, 34
	s_nop 1
	v_writelane_b32 v252, s7, 35
	s_add_u32 s6, s12, 0x4e00
	s_addc_u32 s7, s13, 0
	v_writelane_b32 v252, s6, 36
	s_nop 1
	v_writelane_b32 v252, s7, 37
	s_add_u32 s6, s12, 0x4f00
	s_addc_u32 s7, s13, 0
	v_writelane_b32 v252, s6, 38
	s_nop 1
	v_writelane_b32 v252, s7, 39
	s_add_u32 s6, s12, 0x5000
	s_addc_u32 s7, s13, 0
	v_writelane_b32 v252, s6, 40
	s_nop 1
	v_writelane_b32 v252, s7, 41
	s_add_u32 s6, s12, 0x5100
	s_addc_u32 s7, s13, 0
	v_writelane_b32 v252, s6, 42
	s_nop 1
	v_writelane_b32 v252, s7, 43
	s_add_u32 s6, s12, 0x5200
	s_addc_u32 s7, s13, 0
	v_writelane_b32 v252, s6, 44
	s_nop 1
	v_writelane_b32 v252, s7, 45
	s_add_u32 s6, s12, 0x5300
	s_addc_u32 s7, s13, 0
	v_writelane_b32 v252, s6, 46
	s_cmp_eq_u32 s8, 15
	s_nop 0
	v_writelane_b32 v252, s7, 47
	s_cselect_b64 s[6:7], -1, 0
	v_writelane_b32 v252, s6, 48
	s_cmp_eq_u32 s8, 14
	s_nop 0
	v_writelane_b32 v252, s7, 49
	s_cselect_b64 s[6:7], -1, 0
	v_writelane_b32 v252, s6, 50
	s_cmp_eq_u32 s8, 13
	s_nop 0
	v_writelane_b32 v252, s7, 51
	s_cselect_b64 s[6:7], -1, 0
	v_writelane_b32 v252, s6, 52
	s_cmp_eq_u32 s8, 12
	s_nop 0
	v_writelane_b32 v252, s7, 53
	s_cselect_b64 s[6:7], -1, 0
	v_writelane_b32 v252, s6, 54
	s_cmp_eq_u32 s8, 11
	s_nop 0
	v_writelane_b32 v252, s7, 55
	s_cselect_b64 s[6:7], -1, 0
	v_writelane_b32 v252, s6, 56
	s_cmp_eq_u32 s8, 10
	s_nop 0
	v_writelane_b32 v252, s7, 57
	s_cselect_b64 s[6:7], -1, 0
	v_writelane_b32 v252, s6, 58
	s_cmp_eq_u32 s8, 9
	s_nop 0
	v_writelane_b32 v252, s7, 59
	s_cselect_b64 s[6:7], -1, 0
	v_writelane_b32 v252, s6, 60
	s_cmp_eq_u32 s8, 8
	s_nop 0
	v_writelane_b32 v252, s7, 61
	s_cselect_b64 s[6:7], -1, 0
	v_writelane_b32 v252, s6, 62
	s_cmp_eq_u32 s8, 7
	s_nop 0
	v_writelane_b32 v252, s7, 63
	s_cselect_b64 s[6:7], -1, 0
	v_writelane_b32 v253, s6, 0
	s_cmp_eq_u32 s8, 6
	v_readlane_b32 s11, v252, 0
	v_writelane_b32 v253, s7, 1
	s_cselect_b64 s[6:7], -1, 0
	v_writelane_b32 v253, s6, 2
	s_cmp_eq_u32 s8, 5
	v_readlane_b32 s16, v252, 3
	v_writelane_b32 v253, s7, 3
	s_cselect_b64 s[6:7], -1, 0
	v_writelane_b32 v253, s6, 4
	s_cmp_eq_u32 s8, 4
	v_readlane_b32 s22, v252, 9
	v_writelane_b32 v253, s7, 5
	s_cselect_b64 s[6:7], -1, 0
	v_writelane_b32 v253, s6, 6
	s_cmp_eq_u32 s8, 3
	v_readlane_b32 s23, v252, 10
	v_writelane_b32 v253, s7, 7
	s_cselect_b64 s[6:7], -1, 0
	v_writelane_b32 v253, s6, 8
	s_cmp_eq_u32 s8, 2
	v_readlane_b32 s17, v252, 4
	v_writelane_b32 v253, s7, 9
	s_cselect_b64 s[6:7], -1, 0
	v_writelane_b32 v253, s6, 10
	s_cmp_eq_u32 s8, 1
	v_readlane_b32 s18, v252, 5
	v_writelane_b32 v253, s7, 11
	s_cselect_b64 s[6:7], -1, 0
	v_writelane_b32 v253, s6, 12
	s_cmp_eq_u32 s8, 0
	v_readlane_b32 s19, v252, 6
	v_writelane_b32 v253, s7, 13
	s_cselect_b64 s[6:7], -1, 0
	v_writelane_b32 v253, s6, 14
	v_readlane_b32 s20, v252, 7
	v_readlane_b32 s21, v252, 8
	v_writelane_b32 v253, s7, 15
	s_lshl_b32 s6, s8, 8
	s_add_u32 s4, s4, s6
	s_addc_u32 s5, s5, 0
	s_add_u32 s6, s4, 0x1400
	s_addc_u32 s7, s5, 0
	v_writelane_b32 v253, s6, 16
	s_nop 1
	v_writelane_b32 v253, s7, 17
	s_add_u32 s6, s4, 0x2400
	s_addc_u32 s7, s5, 0
	v_writelane_b32 v253, s6, 18
	s_nop 1
	v_writelane_b32 v253, s7, 19
	s_add_u32 s6, s12, 0x7400
	s_addc_u32 s7, s13, 0
	v_writelane_b32 v253, s6, 20
	s_nop 1
	v_writelane_b32 v253, s7, 21
	s_add_u32 s6, s12, 0x7500
	s_addc_u32 s7, s13, 0
	v_writelane_b32 v253, s6, 22
	s_nop 1
	v_writelane_b32 v253, s7, 23
	s_add_u32 s6, s12, 0x3400000
	s_addc_u32 s7, s13, 0
	v_writelane_b32 v253, s6, 24
	s_nop 1
	v_writelane_b32 v253, s7, 25
	s_mul_i32 s6, s11, 5
	s_add_i32 s6, s6, -3
	s_add_u32 s84, s12, 0x9000
	s_addc_u32 s85, s13, 0
	s_add_u32 s24, s12, 0x1c400000
	s_addc_u32 s25, s13, 0
	v_writelane_b32 v253, s6, 26
	s_add_u32 s6, s12, 0xc00000
; #define PG8_LAS __attribute__((address_space(3)))
; #define LAS __attribute__((address_space(3)))
; __global__ void __launch_bounds__(NTHREADS, 2) mega(MArgs a) {
;     extern __shared__ __attribute__((aligned(16))) unsigned char lds[];
;     PG8_LAS unsigned char* L = (PG8_LAS unsigned char*)lds;
;     unsigned char* ws = a.ws;
;     for (int u = threadIdx.x; u < (MK_LDS_BYTES - LDSCTL_OFF) / 4; u += NTHREADS) ((LAS unsigned*)(L + LDSCTL_OFF))[u] = 0u;
;     __syncthreads();
;     XcdBarrier bar = xcd_barrier_post((unsigned*)(ws + WS_CTL) + CW_BAR, (volatile LAS unsigned*)(L + MISC_OFF) + 8);
;     ...
;             const int vcu = (G % 8 == 0) ? (bx % 8) * (G / 8) + bx / 8 : bx;
	s_addc_u32 s7, s13, 0
	v_writelane_b32 v253, s6, 27
	s_nop 1
	v_writelane_b32 v253, s7, 28
	s_add_u32 s6, s12, 0xa0000
	s_addc_u32 s7, s13, 0
	v_writelane_b32 v253, s6, 29
	s_nop 1
	v_writelane_b32 v253, s7, 30
	s_add_u32 s6, s12, 0x10000
	v_writelane_b32 v253, s6, 31
	s_addc_u32 s6, s13, 0
	s_cmpk_lt_i32 s11, 0x100
	v_writelane_b32 v253, s6, 32
	s_cselect_b64 s[6:7], -1, 0
	v_writelane_b32 v253, s6, 33
	s_nop 1
	v_writelane_b32 v253, s7, 34
	s_ashr_i32 s6, s11, 31
	v_writelane_b32 v253, s6, 35
	s_lshr_b32 s6, s6, 29
	s_add_i32 s6, s11, s6
	s_ashr_i32 s15, s6, 3
	s_and_b32 s6, s6, -8
	s_sub_i32 s26, s11, s6
	s_lshl_b32 s6, s26, 5
	s_add_u32 s0, s38, 0x1000
	v_writelane_b32 v253, s36, 36
	s_addc_u32 s1, s39, 0
	s_nop 0
	v_writelane_b32 v253, s37, 37
	v_writelane_b32 v253, s38, 38
	v_writelane_b32 v253, s39, 39
	v_writelane_b32 v253, s40, 40
	v_writelane_b32 v253, s41, 41
	v_writelane_b32 v253, s42, 42
	v_writelane_b32 v253, s43, 43
	v_writelane_b32 v253, s44, 44
	v_writelane_b32 v253, s45, 45
	v_writelane_b32 v253, s46, 46
	v_writelane_b32 v253, s47, 47
	v_writelane_b32 v253, s48, 48
	v_writelane_b32 v253, s49, 49
	v_writelane_b32 v253, s50, 50
	v_writelane_b32 v253, s51, 51
	v_writelane_b32 v253, s0, 52
	s_mov_b32 s44, 0x800000
	s_mov_b32 s48, 0xe0000
	v_writelane_b32 v253, s1, 53
	s_add_u32 s0, s22, 0x4000000
	s_addc_u32 s1, s23, 0
	v_writelane_b32 v253, s0, 54
	s_mov_b32 s22, 0xfff20000
	s_mov_b32 s49, 0x41400000
	v_writelane_b32 v253, s1, 55
	s_add_u32 s0, s12, 0x1a400000
	v_writelane_b32 v253, s0, 56
	s_addc_u32 s0, s13, 0
	v_writelane_b32 v253, s0, 57
	s_add_u32 s0, s12, 0x5400000
	v_writelane_b32 v253, s0, 58
	s_addc_u32 s0, s13, 0
	v_writelane_b32 v253, s0, 59
	s_add_u32 s0, s12, 0x600000
	s_addc_u32 s1, s13, 0
	v_writelane_b32 v253, s0, 60
	s_mov_b32 s45, s14
	s_mov_b32 s23, -1
	v_writelane_b32 v253, s1, 61
	s_add_u32 s0, s12, 0xc403000
	s_addc_u32 s1, s13, 0
	v_writelane_b32 v253, s0, 62
	s_nop 1
	v_writelane_b32 v253, s1, 63
	s_add_u32 s0, s4, 0x4000
	s_addc_u32 s1, s5, 0
	v_writelane_b32 v254, s0, 0
	s_nop 1
	v_writelane_b32 v254, s1, 1
	s_add_u32 s0, s12, 0xe0000
	s_addc_u32 s1, s13, 0
	s_add_u32 s86, s12, 0x100000
	s_addc_u32 s87, s13, 0
	v_writelane_b32 v254, s0, 2
	s_cmpk_gt_i32 s11, 0xff
	s_nop 0
	v_writelane_b32 v254, s1, 3
	s_cselect_b64 s[0:1], -1, 0
	s_add_u32 s4, s12, 0x1000000
	s_addc_u32 s5, s13, 0
	s_add_u32 s16, s12, 0xc400000
	s_addc_u32 s17, s13, 0
	v_writelane_b32 v254, s4, 4
	s_cmpk_lt_i32 s11, 0x600
	s_nop 0
	v_writelane_b32 v254, s5, 5
	s_cselect_b64 s[4:5], -1, 0
	v_writelane_b32 v254, s4, 6
	s_nop 1
	v_writelane_b32 v254, s5, 7
	s_lshl_b32 s4, s11, 2
	s_add_u32 s88, s12, 0xb400000
	s_addc_u32 s89, s13, 0
	s_add_u32 s79, s12, 0xa400000
	s_addc_u32 s90, s13, 0
	s_add_u32 s92, s12, 0x580000
	s_addc_u32 s93, s13, 0
	s_add_u32 s94, s12, 0x484000
	s_addc_u32 s95, s13, 0
	s_add_u32 s5, s12, 0x300000
	v_writelane_b32 v254, s5, 8
	s_addc_u32 s5, s13, 0
	v_writelane_b32 v254, s5, 9
	s_add_u32 s5, s12, 0x400000
	v_writelane_b32 v254, s5, 10
	s_addc_u32 s5, s13, 0
	v_writelane_b32 v254, s5, 11
	s_add_u32 s5, s12, 0xc401000
	v_writelane_b32 v254, s5, 12
	s_addc_u32 s5, s13, 0
	v_writelane_b32 v254, s5, 13
	s_add_u32 s5, s12, 0xc401400
	v_writelane_b32 v254, s5, 14
	s_addc_u32 s5, s13, 0
	v_writelane_b32 v254, s5, 15
	s_add_u32 s5, s12, 0xc401800
	v_writelane_b32 v254, s5, 16
	s_addc_u32 s5, s13, 0
	v_writelane_b32 v254, s5, 17
	s_add_u32 s5, s12, 0xc401c00
	v_writelane_b32 v254, s5, 18
	s_addc_u32 s5, s13, 0
	v_writelane_b32 v254, s5, 19
	s_add_u32 s5, s12, 0x5400400
	v_writelane_b32 v254, s5, 20
	s_addc_u32 s5, s13, 0
	v_writelane_b32 v254, s5, 21
	s_add_u32 s5, s12, 0xc400400
	v_writelane_b32 v254, s5, 22
	s_addc_u32 s5, s13, 0
	v_writelane_b32 v254, s5, 23
	s_add_u32 s5, s12, 0xc400800
	v_writelane_b32 v254, s5, 24
	s_addc_u32 s5, s13, 0
	v_writelane_b32 v254, s5, 25
	s_add_u32 s5, s12, 0xc400c00
	v_writelane_b32 v254, s5, 26
	s_addc_u32 s5, s13, 0
	v_writelane_b32 v254, s5, 27
	s_add_u32 s5, s12, 0x8400000
	v_writelane_b32 v254, s5, 28
	s_addc_u32 s5, s13, 0
	s_add_u32 s8, s12, 0x500000
	v_writelane_b32 v254, s5, 29
	s_addc_u32 s9, s13, 0
	v_writelane_b32 v254, s8, 30
	s_nop 1
	v_writelane_b32 v254, s9, 31
	s_add_u32 s8, s12, 0x482000
	s_addc_u32 s9, s13, 0
	v_writelane_b32 v254, s8, 32
	s_nop 1
	v_writelane_b32 v254, s9, 33
	s_add_u32 s8, s12, 0x480000
	s_addc_u32 s9, s13, 0
	v_writelane_b32 v254, s8, 34
	s_nop 1
	v_writelane_b32 v254, s9, 35
	s_and_b32 s4, s11, 7
; __global__ void __launch_bounds__(NTHREADS, 2) mega(MArgs a) {
;     ...
;                 if (wv < mlstm::NACT) for (int it = blockIdx.x * mlstm::NACT + wv; it < HB * 128; it += gridDim.x * mlstm::NACT)
;                     mlstm::x1_wave(it, b0, (const h16*)(ws + WS_PROJ), (const float*)(ws + WS_SMALL), a.in[4] + (size_t)layer * 4 * 512, (h16*)(ws + WS_QKC), (h16*)(ws + WS_U),
;                                    (float*)(ws + WS_MUN), (float*)(ws + WS_MAMAX), (float*)(ws + WS_MBLAST), (mlstm::lds_ptr)L + wv * mlstm::WREG, ln);
;                 if (wv >= mlstm::NACT) for (int wq = blockIdx.x * (NWAVES - mlstm::NACT) + (wv - mlstm::NACT); wq < HB * 8 + HB * 64; wq += gridDim.x * (NWAVES - mlstm::NACT)) {
;                     if (wq < HB * 8) fox_cumsum_wave(wq, b0, (const float*)(ws + WS_SMALL), (float*)(ws + WS_CB));
;                     else moba_kmean_wave(wq - HB * 8, b0, (const h16*)(ws + WS_PROJ), (float*)(ws + WS_KMEAN)); }
;     ...
;             const int vcu = (G % 8 == 0) ? (bx % 8) * (G / 8) + bx / 8 : bx;
	s_lshl_b32 s4, s4, 5
	s_lshr_b32 s100, s11, 3
	s_add_i32 s4, s4, s100
	s_lshl_b32 s4, s4, 2
	v_writelane_b32 v254, s4, 36
	s_lshl_b32 s4, s11, 2
	s_add_i32 s4, s4, -4
	v_writelane_b32 v254, s4, 37
	s_lshl_b32 s4, s11, 3
	v_writelane_b32 v254, s4, 38
	s_add_u32 s4, s12, 0x80000
	s_addc_u32 s5, s13, 0
	v_writelane_b32 v254, s4, 39
	s_cmp_lt_i32 s26, 0
	s_nop 0
	v_writelane_b32 v254, s5, 40
	s_mul_i32 s4, s26, 33
	s_cselect_b32 s4, s4, s6
	s_movk_i32 s5, 0xc1
	s_cselect_b32 s6, s5, 0xc0
	s_add_i32 s7, s4, s15
	s_ashr_i32 s8, s7, 31
	s_lshr_b32 s4, s8, 29
	s_add_i32 s4, s7, s4
	s_and_b32 s5, s4, 0xfff8
	s_sub_i32 s5, s7, s5
	s_bfe_u32 s9, s5, 0x10007
	s_add_i32 s9, s5, s9
	s_and_b32 s10, s9, 0xfe
	s_sub_i32 s5, s5, s10
	s_ashr_i32 s4, s4, 3
	s_bfe_i32 s9, s9, 0x80000
	s_lshl_b32 s4, s4, 1
	s_sext_i32_i16 s9, s9
	s_sext_i32_i8 s5, s5
	s_add_i32 s12, s4, s5
	s_ashr_i32 s4, s9, 1
	v_writelane_b32 v254, s4, 41
	s_lshr_b32 s4, s9, 1
	s_bfe_i64 s[4:5], s[4:5], 0x100000
	s_lshl_b64 s[4:5], s[4:5], 19
	v_writelane_b32 v254, s4, 42
	s_ashr_i32 s13, s12, 31
	s_mul_i32 s6, s26, s6
	v_writelane_b32 v254, s5, 43
	s_mov_b32 s4, s12
	v_writelane_b32 v254, s4, 44
	s_nop 1
	v_writelane_b32 v254, s5, 45
	s_lshl_b64 s[4:5], s[12:13], 19
	s_add_u32 s12, s24, s4
	v_writelane_b32 v254, s24, 46
	s_addc_u32 s13, s25, s5
	s_movk_i32 s4, 0x3ff
	v_writelane_b32 v254, s25, 47
	v_and_or_b32 v0, v0, s4, v243
	s_add_u32 s4, s12, 0x40000
	v_writelane_b32 v254, s12, 48
	s_addc_u32 s5, s13, 0
	s_add_i32 s6, s6, s15
	v_writelane_b32 v254, s13, 49
	v_writelane_b32 v254, s4, 50
	s_xor_b64 s[2:3], s[2:3], -1
	s_xor_b64 s[0:1], s[0:1], -1
	v_writelane_b32 v254, s5, 51
	s_lshr_b32 s4, s8, 27
	s_add_i32 s4, s7, s4
	s_and_b32 s5, s4, 0xffe0
	s_sub_i32 s5, s7, s5
	s_bfe_i32 s7, s5, 0x80000
	s_bfe_u32 s7, s7, 0x3000c
	s_add_i32 s7, s5, s7
	s_and_b32 s8, s7, 0xf8
	s_sub_i32 s5, s5, s8
	s_mul_hi_i32 s8, s6, 0x2aaaaaab
	s_lshr_b32 s9, s8, 31
	s_ashr_i32 s8, s8, 4
	s_add_i32 s8, s8, s9
	s_mul_i32 s9, s8, 0x60
	s_sub_i32 s6, s6, s9
	s_bfe_i32 s9, s6, 0x80000
	s_bfe_u32 s9, s9, 0x2000d
	s_add_i32 s9, s6, s9
	s_ashr_i32 s4, s4, 5
	s_and_b32 s10, s9, 0xfc
	s_lshl_b32 s4, s4, 3
	s_sext_i32_i8 s5, s5
	s_sub_i32 s6, s6, s10
	s_add_i32 s12, s4, s5
	s_bfe_i32 s5, s9, 0x80000
	v_writelane_b32 v254, s26, 52
	s_lshl_b32 s4, s8, 2
	s_sext_i32_i16 s5, s5
	s_sext_i32_i8 s6, s6
	v_writelane_b32 v254, s15, 53
	s_add_i32 s8, s4, s6
	s_ashr_i32 s4, s5, 2
	v_writelane_b32 v254, s4, 54
	s_lshr_b32 s4, s5, 2
	s_bfe_i64 s[4:5], s[4:5], 0x100000
	s_bfe_i32 s7, s7, 0x80000
	s_lshl_b64 s[4:5], s[4:5], 19
	s_sext_i32_i16 s7, s7
	v_writelane_b32 v254, s4, 55
	s_ashr_i32 s9, s8, 31
	s_ashr_i32 s13, s12, 31
	v_writelane_b32 v254, s5, 56
	s_ashr_i32 s4, s7, 3
	v_writelane_b32 v254, s4, 57
	s_lshr_b32 s4, s7, 3
	s_bfe_i64 s[4:5], s[4:5], 0x100000
	s_lshl_b64 s[4:5], s[4:5], 19
	v_writelane_b32 v254, s4, 58
	s_mov_b32 s24, 0xffe40000
	s_movk_i32 s7, 0xc00
	v_writelane_b32 v254, s5, 59
	s_mul_i32 s4, s11, 10
	s_add_i32 s4, s4, -5
	v_writelane_b32 v254, s4, 60
	v_writelane_b32 v254, s2, 61
	s_add_i32 s33, 0, 0x14800
	s_mov_b32 s25, -1
	v_writelane_b32 v254, s3, 62
	v_writelane_b32 v254, s0, 63
	s_nop 1
	v_writelane_b32 v255, s1, 0
	s_lshl_b32 s0, s11, 4
	v_writelane_b32 v255, s0, 1
	s_add_i32 s0, 0, 0x20160
	v_writelane_b32 v255, s0, 2
	s_add_i32 s0, 0, 0x20164
	v_writelane_b32 v255, s0, 3
	s_add_i32 s0, 0, 0x15000
	v_writelane_b32 v255, s0, 4
	v_cmp_eq_u32_e64 s[0:1], 0, v0
	s_nop 1
	v_writelane_b32 v255, s0, 5
	s_nop 1
	v_writelane_b32 v255, s1, 6
	s_mov_b32 s0, s8
	v_writelane_b32 v255, s0, 7
	s_nop 1
	v_writelane_b32 v255, s1, 8
	s_lshl_b64 s[0:1], s[8:9], 19
	v_writelane_b32 v255, s0, 9
	s_mov_b64 s[8:9], 0x1c0000
	s_nop 0
	v_writelane_b32 v255, s1, 10
	s_mov_b32 s0, s12
	v_writelane_b32 v255, s0, 11
	s_nop 1
	v_writelane_b32 v255, s1, 12
	s_lshl_b64 s[0:1], s[12:13], 19
	v_writelane_b32 v255, s0, 13
	s_nop 1
	v_writelane_b32 v255, s1, 14
	v_writelane_b32 v255, s80, 15
	s_nop 1
	v_writelane_b32 v255, s81, 16
	v_writelane_b32 v255, s82, 17
	s_nop 1
	v_writelane_b32 v255, s83, 18
	v_writelane_b32 v255, s84, 19
	s_nop 1
	v_writelane_b32 v255, s85, 20
	v_writelane_b32 v255, s86, 21
	s_nop 1
	v_writelane_b32 v255, s87, 22
	v_writelane_b32 v255, s88, 23
	s_nop 1
	v_writelane_b32 v255, s89, 24
	v_writelane_b32 v255, s79, 25
	v_writelane_b32 v255, s90, 26
	v_writelane_b32 v255, s92, 27
	v_writelane_b32 v255, s93, 28
	v_writelane_b32 v255, s94, 29
	v_writelane_b32 v255, s95, 30
	s_branch .LBB0_16
